# grid barriers after phases whose stores are all 16-byte write-through (proj, prep, LoRA GEMM, post, w_out): no buffer_wbl2 on the release chain (drain + flag, as the write-through hand-off recipe)
# speedup vs baseline: 1.0022x; 1.0022x over previous
.LBB0_404:
	s_andn2_saveexec_b64 s[6:7], s[6:7]
	s_cbranch_execz .LBB0_424
	s_mov_b64 s[6:7], exec
	s_waitcnt lgkmcnt(0)
	s_waitcnt vmcnt(0)
	v_mbcnt_lo_u32_b32 v0, s6, 0
	v_mbcnt_hi_u32_b32 v0, s7, v0
	v_cmp_eq_u32_e32 vcc, 0, v0
	s_and_saveexec_b64 s[8:9], vcc
	s_cbranch_execz .LBB0_407
	s_bcnt1_i32_b64 s6, s[6:7]
	v_mov_b32_e32 v3, s6
	v_readlane_b32 s6, v254, 7
	v_readlane_b32 s7, v254, 8
	s_nop 4
	global_atomic_add v3, v1, v3, s[6:7] sc0
